# speedup vs baseline: 1.0023x; 1.0023x over previous
.Lup_loop:
	s_waitcnt lgkmcnt(0)
	v_mfma_f32_16x16x32_bf16 v[128:131], v[48:51], v[32:35], v[128:131]
	ds_read_b128 v[80:83], v13 offset:0
	v_mfma_f32_16x16x32_bf16 v[132:135], v[48:51], v[36:39], v[132:135]
	ds_read_b128 v[84:87], v13 offset:2048
	v_mfma_f32_16x16x32_bf16 v[136:139], v[48:51], v[40:43], v[136:139]
	ds_read_b128 v[88:91], v13 offset:4096
	v_mfma_f32_16x16x32_bf16 v[140:143], v[48:51], v[44:47], v[140:143]
	ds_read_b128 v[92:95], v13 offset:6144
	v_mfma_f32_16x16x32_bf16 v[144:147], v[52:55], v[32:35], v[144:147]
	ds_read_b128 v[96:99], v15 offset:0
	v_mfma_f32_16x16x32_bf16 v[148:151], v[52:55], v[36:39], v[148:151]
	ds_read_b128 v[100:103], v15 offset:2048
	v_mfma_f32_16x16x32_bf16 v[152:155], v[52:55], v[40:43], v[152:155]
	ds_read_b128 v[104:107], v15 offset:4096
	v_mfma_f32_16x16x32_bf16 v[156:159], v[52:55], v[44:47], v[156:159]
	ds_read_b128 v[108:111], v15 offset:6144
	v_mfma_f32_16x16x32_bf16 v[160:163], v[56:59], v[32:35], v[160:163]
	ds_read_b128 v[112:115], v15 offset:8192
	v_mfma_f32_16x16x32_bf16 v[164:167], v[56:59], v[36:39], v[164:167]
	ds_read_b128 v[116:119], v15 offset:10240
	v_mfma_f32_16x16x32_bf16 v[168:171], v[56:59], v[40:43], v[168:171]
	ds_read_b128 v[120:123], v15 offset:12288
	v_mfma_f32_16x16x32_bf16 v[172:175], v[56:59], v[44:47], v[172:175]
	ds_read_b128 v[124:127], v15 offset:14336
	v_mfma_f32_16x16x32_bf16 v[176:179], v[60:63], v[32:35], v[176:179]
	s_add_u32 m0, s20, 0x6000
	v_mfma_f32_16x16x32_bf16 v[180:183], v[60:63], v[36:39], v[180:183]
	global_load_lds_dwordx4 v4, s[18:19]
	v_mfma_f32_16x16x32_bf16 v[184:187], v[60:63], v[40:43], v[184:187]
	s_add_u32 m0, s20, 0x7000
	v_mfma_f32_16x16x32_bf16 v[188:191], v[60:63], v[44:47], v[188:191]
	global_load_lds_dwordx4 v5, s[18:19]
	v_mfma_f32_16x16x32_bf16 v[192:195], v[64:67], v[32:35], v[192:195]
	s_add_u32 m0, s20, 0x8000
	v_mfma_f32_16x16x32_bf16 v[196:199], v[64:67], v[36:39], v[196:199]
	global_load_lds_dwordx4 v6, s[18:19]
	v_mfma_f32_16x16x32_bf16 v[200:203], v[64:67], v[40:43], v[200:203]
	s_add_u32 m0, s20, 0x9000
	v_mfma_f32_16x16x32_bf16 v[204:207], v[64:67], v[44:47], v[204:207]
	global_load_lds_dwordx4 v7, s[18:19]
	v_mfma_f32_16x16x32_bf16 v[208:211], v[68:71], v[32:35], v[208:211]
	s_add_u32 m0, s20, 0xa000
	v_mfma_f32_16x16x32_bf16 v[212:215], v[68:71], v[36:39], v[212:215]
	global_load_lds_dwordx4 v8, s[18:19]
	v_mfma_f32_16x16x32_bf16 v[216:219], v[68:71], v[40:43], v[216:219]
	s_add_u32 m0, s20, 0xb000
	v_mfma_f32_16x16x32_bf16 v[220:223], v[68:71], v[44:47], v[220:223]
	global_load_lds_dwordx4 v9, s[18:19]
	v_mfma_f32_16x16x32_bf16 v[224:227], v[72:75], v[32:35], v[224:227]
	v_mfma_f32_16x16x32_bf16 v[228:231], v[72:75], v[36:39], v[228:231]
	v_mfma_f32_16x16x32_bf16 v[232:235], v[72:75], v[40:43], v[232:235]
	v_mfma_f32_16x16x32_bf16 v[236:239], v[72:75], v[44:47], v[236:239]
	v_mfma_f32_16x16x32_bf16 v[240:243], v[76:79], v[32:35], v[240:243]
	s_add_u32 s16, s16, 0x80
	s_addc_u32 s17, s17, 0
	s_add_u32 s18, s18, 0x80
	s_addc_u32 s19, s19, 0
	v_mfma_f32_16x16x32_bf16 v[244:247], v[76:79], v[36:39], v[244:247]
	s_add_u32 s20, s20, 0xc000
	s_sub_u32 s22, s20, 0x24000
	s_cmp_ge_u32 s20, 0x24000
	s_cselect_b32 s20, s22, s20
	v_mfma_f32_16x16x32_bf16 v[248:251], v[76:79], v[40:43], v[248:251]
	v_add_u32_e32 v12, s21, v10
	v_add_u32_e32 v14, s21, v11
	v_xor_b32_e32 v13, 64, v12
	v_xor_b32_e32 v15, 64, v14
	v_mfma_f32_16x16x32_bf16 v[252:255], v[76:79], v[44:47], v[252:255]
	s_add_u32 s21, s21, 0xc000
	s_sub_u32 s23, s21, 0x24000
	s_cmp_ge_u32 s21, 0x24000
	s_cselect_b32 s21, s23, s21
	s_waitcnt lgkmcnt(0)
	v_mfma_f32_16x16x32_bf16 v[128:131], v[96:99], v[80:83], v[128:131]
	v_mfma_f32_16x16x32_bf16 v[132:135], v[96:99], v[84:87], v[132:135]
	v_mfma_f32_16x16x32_bf16 v[136:139], v[96:99], v[88:91], v[136:139]
	v_mfma_f32_16x16x32_bf16 v[140:143], v[96:99], v[92:95], v[140:143]
	v_mfma_f32_16x16x32_bf16 v[144:147], v[100:103], v[80:83], v[144:147]
	v_mfma_f32_16x16x32_bf16 v[148:151], v[100:103], v[84:87], v[148:151]
	v_mfma_f32_16x16x32_bf16 v[152:155], v[100:103], v[88:91], v[152:155]
	v_mfma_f32_16x16x32_bf16 v[156:159], v[100:103], v[92:95], v[156:159]
	s_waitcnt vmcnt(12)
	s_barrier
	v_mfma_f32_16x16x32_bf16 v[160:163], v[104:107], v[80:83], v[160:163]
	ds_read_b128 v[32:35], v12 offset:0
	v_mfma_f32_16x16x32_bf16 v[164:167], v[104:107], v[84:87], v[164:167]
	ds_read_b128 v[36:39], v12 offset:2048
	v_mfma_f32_16x16x32_bf16 v[168:171], v[104:107], v[88:91], v[168:171]
	ds_read_b128 v[40:43], v12 offset:4096
	v_mfma_f32_16x16x32_bf16 v[172:175], v[104:107], v[92:95], v[172:175]
	ds_read_b128 v[44:47], v12 offset:6144
	v_mfma_f32_16x16x32_bf16 v[176:179], v[108:111], v[80:83], v[176:179]
	ds_read_b128 v[48:51], v14 offset:0
	v_mfma_f32_16x16x32_bf16 v[180:183], v[108:111], v[84:87], v[180:183]
	ds_read_b128 v[52:55], v14 offset:2048
	v_mfma_f32_16x16x32_bf16 v[184:187], v[108:111], v[88:91], v[184:187]
	ds_read_b128 v[56:59], v14 offset:4096
	v_mfma_f32_16x16x32_bf16 v[188:191], v[108:111], v[92:95], v[188:191]
	ds_read_b128 v[60:63], v14 offset:6144
	v_mfma_f32_16x16x32_bf16 v[192:195], v[112:115], v[80:83], v[192:195]
	ds_read_b128 v[64:67], v14 offset:8192
	v_mfma_f32_16x16x32_bf16 v[196:199], v[112:115], v[84:87], v[196:199]
	ds_read_b128 v[68:71], v14 offset:10240
	v_mfma_f32_16x16x32_bf16 v[200:203], v[112:115], v[88:91], v[200:203]
	ds_read_b128 v[72:75], v14 offset:12288
	v_mfma_f32_16x16x32_bf16 v[204:207], v[112:115], v[92:95], v[204:207]
	ds_read_b128 v[76:79], v14 offset:14336
	v_mfma_f32_16x16x32_bf16 v[208:211], v[116:119], v[80:83], v[208:211]
	s_add_u32 m0, s20, 0x0
	v_mfma_f32_16x16x32_bf16 v[212:215], v[116:119], v[84:87], v[212:215]
	global_load_lds_dwordx4 v2, s[16:17]
	v_mfma_f32_16x16x32_bf16 v[216:219], v[116:119], v[88:91], v[216:219]
	s_add_u32 m0, s20, 0x1000
	v_mfma_f32_16x16x32_bf16 v[220:223], v[116:119], v[92:95], v[220:223]
	global_load_lds_dwordx4 v3, s[16:17]
	v_mfma_f32_16x16x32_bf16 v[224:227], v[120:123], v[80:83], v[224:227]
	s_add_u32 m0, s20, 0x2000
	v_mfma_f32_16x16x32_bf16 v[228:231], v[120:123], v[84:87], v[228:231]
	global_load_lds_dwordx4 v4, s[16:17]
	v_mfma_f32_16x16x32_bf16 v[232:235], v[120:123], v[88:91], v[232:235]
	s_add_u32 m0, s20, 0x3000
	v_mfma_f32_16x16x32_bf16 v[236:239], v[120:123], v[92:95], v[236:239]
	global_load_lds_dwordx4 v5, s[16:17]
	v_mfma_f32_16x16x32_bf16 v[240:243], v[124:127], v[80:83], v[240:243]
	s_add_u32 m0, s20, 0x4000
	v_mfma_f32_16x16x32_bf16 v[244:247], v[124:127], v[84:87], v[244:247]
	global_load_lds_dwordx4 v2, s[18:19]
	v_mfma_f32_16x16x32_bf16 v[248:251], v[124:127], v[88:91], v[248:251]
	s_add_u32 m0, s20, 0x5000
	v_mfma_f32_16x16x32_bf16 v[252:255], v[124:127], v[92:95], v[252:255]
	global_load_lds_dwordx4 v3, s[18:19]
	s_add_u32 s15, s15, 1
	s_cmp_lt_u32 s15, 9
	s_cbranch_scc1 .Lup_loop
	s_waitcnt lgkmcnt(0)
	v_mfma_f32_16x16x32_bf16 v[128:131], v[48:51], v[32:35], v[128:131]
	ds_read_b128 v[80:83], v13 offset:0
	v_mfma_f32_16x16x32_bf16 v[132:135], v[48:51], v[36:39], v[132:135]
	ds_read_b128 v[84:87], v13 offset:2048
	v_mfma_f32_16x16x32_bf16 v[136:139], v[48:51], v[40:43], v[136:139]
	ds_read_b128 v[88:91], v13 offset:4096
	v_mfma_f32_16x16x32_bf16 v[140:143], v[48:51], v[44:47], v[140:143]
	ds_read_b128 v[92:95], v13 offset:6144
	v_mfma_f32_16x16x32_bf16 v[144:147], v[52:55], v[32:35], v[144:147]
	ds_read_b128 v[96:99], v15 offset:0
	v_mfma_f32_16x16x32_bf16 v[148:151], v[52:55], v[36:39], v[148:151]
	ds_read_b128 v[100:103], v15 offset:2048
	v_mfma_f32_16x16x32_bf16 v[152:155], v[52:55], v[40:43], v[152:155]
	ds_read_b128 v[104:107], v15 offset:4096
	v_mfma_f32_16x16x32_bf16 v[156:159], v[52:55], v[44:47], v[156:159]
	ds_read_b128 v[108:111], v15 offset:6144
	v_mfma_f32_16x16x32_bf16 v[160:163], v[56:59], v[32:35], v[160:163]
	ds_read_b128 v[112:115], v15 offset:8192
	v_mfma_f32_16x16x32_bf16 v[164:167], v[56:59], v[36:39], v[164:167]
	ds_read_b128 v[116:119], v15 offset:10240
	v_mfma_f32_16x16x32_bf16 v[168:171], v[56:59], v[40:43], v[168:171]
	ds_read_b128 v[120:123], v15 offset:12288
	v_mfma_f32_16x16x32_bf16 v[172:175], v[56:59], v[44:47], v[172:175]
	ds_read_b128 v[124:127], v15 offset:14336
	v_mfma_f32_16x16x32_bf16 v[176:179], v[60:63], v[32:35], v[176:179]
	s_add_u32 m0, s20, 0x6000
	v_mfma_f32_16x16x32_bf16 v[180:183], v[60:63], v[36:39], v[180:183]
	global_load_lds_dwordx4 v4, s[18:19]
	v_mfma_f32_16x16x32_bf16 v[184:187], v[60:63], v[40:43], v[184:187]
	s_add_u32 m0, s20, 0x7000
	v_mfma_f32_16x16x32_bf16 v[188:191], v[60:63], v[44:47], v[188:191]
	global_load_lds_dwordx4 v5, s[18:19]
	v_mfma_f32_16x16x32_bf16 v[192:195], v[64:67], v[32:35], v[192:195]
	s_add_u32 m0, s20, 0x8000
	v_mfma_f32_16x16x32_bf16 v[196:199], v[64:67], v[36:39], v[196:199]
	global_load_lds_dwordx4 v6, s[18:19]
	v_mfma_f32_16x16x32_bf16 v[200:203], v[64:67], v[40:43], v[200:203]
	s_add_u32 m0, s20, 0x9000
	v_mfma_f32_16x16x32_bf16 v[204:207], v[64:67], v[44:47], v[204:207]
	global_load_lds_dwordx4 v7, s[18:19]
	v_mfma_f32_16x16x32_bf16 v[208:211], v[68:71], v[32:35], v[208:211]
	s_add_u32 m0, s20, 0xa000
	v_mfma_f32_16x16x32_bf16 v[212:215], v[68:71], v[36:39], v[212:215]
	global_load_lds_dwordx4 v8, s[18:19]
	v_mfma_f32_16x16x32_bf16 v[216:219], v[68:71], v[40:43], v[216:219]
	s_add_u32 m0, s20, 0xb000
	v_mfma_f32_16x16x32_bf16 v[220:223], v[68:71], v[44:47], v[220:223]
	global_load_lds_dwordx4 v9, s[18:19]
	v_mfma_f32_16x16x32_bf16 v[224:227], v[72:75], v[32:35], v[224:227]
	v_mfma_f32_16x16x32_bf16 v[228:231], v[72:75], v[36:39], v[228:231]
	v_mfma_f32_16x16x32_bf16 v[232:235], v[72:75], v[40:43], v[232:235]
	v_mfma_f32_16x16x32_bf16 v[236:239], v[72:75], v[44:47], v[236:239]
	v_mfma_f32_16x16x32_bf16 v[240:243], v[76:79], v[32:35], v[240:243]
	s_add_u32 s16, s16, 0x80
	s_addc_u32 s17, s17, 0
	s_add_u32 s18, s18, 0x80
	s_addc_u32 s19, s19, 0
	v_mfma_f32_16x16x32_bf16 v[244:247], v[76:79], v[36:39], v[244:247]
	s_add_u32 s20, s20, 0xc000
	s_sub_u32 s22, s20, 0x24000
	s_cmp_ge_u32 s20, 0x24000
	s_cselect_b32 s20, s22, s20
	v_mfma_f32_16x16x32_bf16 v[248:251], v[76:79], v[40:43], v[248:251]
	v_add_u32_e32 v12, s21, v10
	v_add_u32_e32 v14, s21, v11
	v_xor_b32_e32 v13, 64, v12
	v_xor_b32_e32 v15, 64, v14
	v_mfma_f32_16x16x32_bf16 v[252:255], v[76:79], v[44:47], v[252:255]
	s_add_u32 s21, s21, 0xc000
	s_sub_u32 s23, s21, 0x24000
	s_cmp_ge_u32 s21, 0x24000
	s_cselect_b32 s21, s23, s21
	s_waitcnt lgkmcnt(0)
	v_mfma_f32_16x16x32_bf16 v[128:131], v[96:99], v[80:83], v[128:131]
	v_mfma_f32_16x16x32_bf16 v[132:135], v[96:99], v[84:87], v[132:135]
	v_mfma_f32_16x16x32_bf16 v[136:139], v[96:99], v[88:91], v[136:139]
	v_mfma_f32_16x16x32_bf16 v[140:143], v[96:99], v[92:95], v[140:143]
	v_mfma_f32_16x16x32_bf16 v[144:147], v[100:103], v[80:83], v[144:147]
	v_mfma_f32_16x16x32_bf16 v[148:151], v[100:103], v[84:87], v[148:151]
	v_mfma_f32_16x16x32_bf16 v[152:155], v[100:103], v[88:91], v[152:155]
	v_mfma_f32_16x16x32_bf16 v[156:159], v[100:103], v[92:95], v[156:159]
	s_waitcnt vmcnt(12)
	s_barrier
	v_mfma_f32_16x16x32_bf16 v[160:163], v[104:107], v[80:83], v[160:163]
	ds_read_b128 v[32:35], v12 offset:0
	v_mfma_f32_16x16x32_bf16 v[164:167], v[104:107], v[84:87], v[164:167]
	ds_read_b128 v[36:39], v12 offset:2048
	v_mfma_f32_16x16x32_bf16 v[168:171], v[104:107], v[88:91], v[168:171]
	ds_read_b128 v[40:43], v12 offset:4096
	v_mfma_f32_16x16x32_bf16 v[172:175], v[104:107], v[92:95], v[172:175]
	ds_read_b128 v[44:47], v12 offset:6144
	v_mfma_f32_16x16x32_bf16 v[176:179], v[108:111], v[80:83], v[176:179]
	ds_read_b128 v[48:51], v14 offset:0
	v_mfma_f32_16x16x32_bf16 v[180:183], v[108:111], v[84:87], v[180:183]
	ds_read_b128 v[52:55], v14 offset:2048
	v_mfma_f32_16x16x32_bf16 v[184:187], v[108:111], v[88:91], v[184:187]
	ds_read_b128 v[56:59], v14 offset:4096
	v_mfma_f32_16x16x32_bf16 v[188:191], v[108:111], v[92:95], v[188:191]
	ds_read_b128 v[60:63], v14 offset:6144
	v_mfma_f32_16x16x32_bf16 v[192:195], v[112:115], v[80:83], v[192:195]
	ds_read_b128 v[64:67], v14 offset:8192
	v_mfma_f32_16x16x32_bf16 v[196:199], v[112:115], v[84:87], v[196:199]
	ds_read_b128 v[68:71], v14 offset:10240
	v_mfma_f32_16x16x32_bf16 v[200:203], v[112:115], v[88:91], v[200:203]
	ds_read_b128 v[72:75], v14 offset:12288
	v_mfma_f32_16x16x32_bf16 v[204:207], v[112:115], v[92:95], v[204:207]
	ds_read_b128 v[76:79], v14 offset:14336
	v_mfma_f32_16x16x32_bf16 v[208:211], v[116:119], v[80:83], v[208:211]
	v_mfma_f32_16x16x32_bf16 v[212:215], v[116:119], v[84:87], v[212:215]
	v_mfma_f32_16x16x32_bf16 v[216:219], v[116:119], v[88:91], v[216:219]
	v_mfma_f32_16x16x32_bf16 v[220:223], v[116:119], v[92:95], v[220:223]
	v_mfma_f32_16x16x32_bf16 v[224:227], v[120:123], v[80:83], v[224:227]
	v_mfma_f32_16x16x32_bf16 v[228:231], v[120:123], v[84:87], v[228:231]
	v_mfma_f32_16x16x32_bf16 v[232:235], v[120:123], v[88:91], v[232:235]
	v_mfma_f32_16x16x32_bf16 v[236:239], v[120:123], v[92:95], v[236:239]
	v_mfma_f32_16x16x32_bf16 v[240:243], v[124:127], v[80:83], v[240:243]
	v_mfma_f32_16x16x32_bf16 v[244:247], v[124:127], v[84:87], v[244:247]
	v_mfma_f32_16x16x32_bf16 v[248:251], v[124:127], v[88:91], v[248:251]
	v_mfma_f32_16x16x32_bf16 v[252:255], v[124:127], v[92:95], v[252:255]
	s_waitcnt lgkmcnt(0)
	v_mfma_f32_16x16x32_bf16 v[128:131], v[48:51], v[32:35], v[128:131]
	ds_read_b128 v[80:83], v13 offset:0
	v_mfma_f32_16x16x32_bf16 v[132:135], v[48:51], v[36:39], v[132:135]
	ds_read_b128 v[84:87], v13 offset:2048
	v_mfma_f32_16x16x32_bf16 v[136:139], v[48:51], v[40:43], v[136:139]
	ds_read_b128 v[88:91], v13 offset:4096
	v_mfma_f32_16x16x32_bf16 v[140:143], v[48:51], v[44:47], v[140:143]
	ds_read_b128 v[92:95], v13 offset:6144
	v_mfma_f32_16x16x32_bf16 v[144:147], v[52:55], v[32:35], v[144:147]
	ds_read_b128 v[96:99], v15 offset:0
	v_mfma_f32_16x16x32_bf16 v[148:151], v[52:55], v[36:39], v[148:151]
	ds_read_b128 v[100:103], v15 offset:2048
	v_mfma_f32_16x16x32_bf16 v[152:155], v[52:55], v[40:43], v[152:155]
	ds_read_b128 v[104:107], v15 offset:4096
	v_mfma_f32_16x16x32_bf16 v[156:159], v[52:55], v[44:47], v[156:159]
	ds_read_b128 v[108:111], v15 offset:6144
	v_mfma_f32_16x16x32_bf16 v[160:163], v[56:59], v[32:35], v[160:163]
	ds_read_b128 v[112:115], v15 offset:8192
	v_mfma_f32_16x16x32_bf16 v[164:167], v[56:59], v[36:39], v[164:167]
	ds_read_b128 v[116:119], v15 offset:10240
	v_mfma_f32_16x16x32_bf16 v[168:171], v[56:59], v[40:43], v[168:171]
	ds_read_b128 v[120:123], v15 offset:12288
	v_mfma_f32_16x16x32_bf16 v[172:175], v[56:59], v[44:47], v[172:175]
	ds_read_b128 v[124:127], v15 offset:14336
	v_mfma_f32_16x16x32_bf16 v[176:179], v[60:63], v[32:35], v[176:179]
	v_mfma_f32_16x16x32_bf16 v[180:183], v[60:63], v[36:39], v[180:183]
	v_mfma_f32_16x16x32_bf16 v[184:187], v[60:63], v[40:43], v[184:187]
	v_mfma_f32_16x16x32_bf16 v[188:191], v[60:63], v[44:47], v[188:191]
	v_mfma_f32_16x16x32_bf16 v[192:195], v[64:67], v[32:35], v[192:195]
	v_mfma_f32_16x16x32_bf16 v[196:199], v[64:67], v[36:39], v[196:199]
	v_mfma_f32_16x16x32_bf16 v[200:203], v[64:67], v[40:43], v[200:203]
	v_mfma_f32_16x16x32_bf16 v[204:207], v[64:67], v[44:47], v[204:207]
	v_mfma_f32_16x16x32_bf16 v[208:211], v[68:71], v[32:35], v[208:211]
	v_mfma_f32_16x16x32_bf16 v[212:215], v[68:71], v[36:39], v[212:215]
	v_mfma_f32_16x16x32_bf16 v[216:219], v[68:71], v[40:43], v[216:219]
	v_mfma_f32_16x16x32_bf16 v[220:223], v[68:71], v[44:47], v[220:223]
	v_mfma_f32_16x16x32_bf16 v[224:227], v[72:75], v[32:35], v[224:227]
	v_mfma_f32_16x16x32_bf16 v[228:231], v[72:75], v[36:39], v[228:231]
	v_mfma_f32_16x16x32_bf16 v[232:235], v[72:75], v[40:43], v[232:235]
	v_mfma_f32_16x16x32_bf16 v[236:239], v[72:75], v[44:47], v[236:239]
	v_mfma_f32_16x16x32_bf16 v[240:243], v[76:79], v[32:35], v[240:243]
	v_add_u32_e32 v12, s21, v10
	v_add_u32_e32 v14, s21, v11
	v_xor_b32_e32 v13, 64, v12
	v_xor_b32_e32 v15, 64, v14
	v_mfma_f32_16x16x32_bf16 v[244:247], v[76:79], v[36:39], v[244:247]
	s_add_u32 s21, s21, 0xc000
	s_sub_u32 s23, s21, 0x24000
	s_cmp_ge_u32 s21, 0x24000
	s_cselect_b32 s21, s23, s21
	v_mfma_f32_16x16x32_bf16 v[248:251], v[76:79], v[40:43], v[248:251]
	v_mfma_f32_16x16x32_bf16 v[252:255], v[76:79], v[44:47], v[252:255]
	s_waitcnt lgkmcnt(0)
	v_mfma_f32_16x16x32_bf16 v[128:131], v[96:99], v[80:83], v[128:131]
	v_mfma_f32_16x16x32_bf16 v[132:135], v[96:99], v[84:87], v[132:135]
	v_mfma_f32_16x16x32_bf16 v[136:139], v[96:99], v[88:91], v[136:139]
	v_mfma_f32_16x16x32_bf16 v[140:143], v[96:99], v[92:95], v[140:143]
	v_mfma_f32_16x16x32_bf16 v[144:147], v[100:103], v[80:83], v[144:147]
	v_mfma_f32_16x16x32_bf16 v[148:151], v[100:103], v[84:87], v[148:151]
	v_mfma_f32_16x16x32_bf16 v[152:155], v[100:103], v[88:91], v[152:155]
	v_mfma_f32_16x16x32_bf16 v[156:159], v[100:103], v[92:95], v[156:159]
	s_waitcnt vmcnt(0)
	s_barrier
	v_mfma_f32_16x16x32_bf16 v[160:163], v[104:107], v[80:83], v[160:163]
	ds_read_b128 v[32:35], v12 offset:0
	v_mfma_f32_16x16x32_bf16 v[164:167], v[104:107], v[84:87], v[164:167]
	ds_read_b128 v[36:39], v12 offset:2048
	v_mfma_f32_16x16x32_bf16 v[168:171], v[104:107], v[88:91], v[168:171]
	ds_read_b128 v[40:43], v12 offset:4096
	v_mfma_f32_16x16x32_bf16 v[172:175], v[104:107], v[92:95], v[172:175]
	ds_read_b128 v[44:47], v12 offset:6144
	v_mfma_f32_16x16x32_bf16 v[176:179], v[108:111], v[80:83], v[176:179]
	ds_read_b128 v[48:51], v14 offset:0
	v_mfma_f32_16x16x32_bf16 v[180:183], v[108:111], v[84:87], v[180:183]
	ds_read_b128 v[52:55], v14 offset:2048
	v_mfma_f32_16x16x32_bf16 v[184:187], v[108:111], v[88:91], v[184:187]
	ds_read_b128 v[56:59], v14 offset:4096
	v_mfma_f32_16x16x32_bf16 v[188:191], v[108:111], v[92:95], v[188:191]
	ds_read_b128 v[60:63], v14 offset:6144
	v_mfma_f32_16x16x32_bf16 v[192:195], v[112:115], v[80:83], v[192:195]
	ds_read_b128 v[64:67], v14 offset:8192
	v_mfma_f32_16x16x32_bf16 v[196:199], v[112:115], v[84:87], v[196:199]
	ds_read_b128 v[68:71], v14 offset:10240
	v_mfma_f32_16x16x32_bf16 v[200:203], v[112:115], v[88:91], v[200:203]
	ds_read_b128 v[72:75], v14 offset:12288
	v_mfma_f32_16x16x32_bf16 v[204:207], v[112:115], v[92:95], v[204:207]
	ds_read_b128 v[76:79], v14 offset:14336
	v_mfma_f32_16x16x32_bf16 v[208:211], v[116:119], v[80:83], v[208:211]
	v_mfma_f32_16x16x32_bf16 v[212:215], v[116:119], v[84:87], v[212:215]
	v_mfma_f32_16x16x32_bf16 v[216:219], v[116:119], v[88:91], v[216:219]
	v_mfma_f32_16x16x32_bf16 v[220:223], v[116:119], v[92:95], v[220:223]
	v_mfma_f32_16x16x32_bf16 v[224:227], v[120:123], v[80:83], v[224:227]
	v_mfma_f32_16x16x32_bf16 v[228:231], v[120:123], v[84:87], v[228:231]
	v_mfma_f32_16x16x32_bf16 v[232:235], v[120:123], v[88:91], v[232:235]
	v_mfma_f32_16x16x32_bf16 v[236:239], v[120:123], v[92:95], v[236:239]
	v_mfma_f32_16x16x32_bf16 v[240:243], v[124:127], v[80:83], v[240:243]
	v_mfma_f32_16x16x32_bf16 v[244:247], v[124:127], v[84:87], v[244:247]
	v_mfma_f32_16x16x32_bf16 v[248:251], v[124:127], v[88:91], v[248:251]
	v_mfma_f32_16x16x32_bf16 v[252:255], v[124:127], v[92:95], v[252:255]
	s_waitcnt lgkmcnt(0)
	v_mfma_f32_16x16x32_bf16 v[128:131], v[48:51], v[32:35], v[128:131]
	ds_read_b128 v[80:83], v13 offset:0
	v_mfma_f32_16x16x32_bf16 v[132:135], v[48:51], v[36:39], v[132:135]
	ds_read_b128 v[84:87], v13 offset:2048
	v_mfma_f32_16x16x32_bf16 v[136:139], v[48:51], v[40:43], v[136:139]
	ds_read_b128 v[88:91], v13 offset:4096
	v_mfma_f32_16x16x32_bf16 v[140:143], v[48:51], v[44:47], v[140:143]
	ds_read_b128 v[92:95], v13 offset:6144
	v_mfma_f32_16x16x32_bf16 v[144:147], v[52:55], v[32:35], v[144:147]
	ds_read_b128 v[96:99], v15 offset:0
	v_mfma_f32_16x16x32_bf16 v[148:151], v[52:55], v[36:39], v[148:151]
	ds_read_b128 v[100:103], v15 offset:2048
	v_mfma_f32_16x16x32_bf16 v[152:155], v[52:55], v[40:43], v[152:155]
	ds_read_b128 v[104:107], v15 offset:4096
	v_mfma_f32_16x16x32_bf16 v[156:159], v[52:55], v[44:47], v[156:159]
	ds_read_b128 v[108:111], v15 offset:6144
	v_mfma_f32_16x16x32_bf16 v[160:163], v[56:59], v[32:35], v[160:163]
	ds_read_b128 v[112:115], v15 offset:8192
	v_mfma_f32_16x16x32_bf16 v[164:167], v[56:59], v[36:39], v[164:167]
	ds_read_b128 v[116:119], v15 offset:10240
	v_mfma_f32_16x16x32_bf16 v[168:171], v[56:59], v[40:43], v[168:171]
	ds_read_b128 v[120:123], v15 offset:12288
	v_mfma_f32_16x16x32_bf16 v[172:175], v[56:59], v[44:47], v[172:175]
	ds_read_b128 v[124:127], v15 offset:14336
	v_mfma_f32_16x16x32_bf16 v[176:179], v[60:63], v[32:35], v[176:179]
	v_mfma_f32_16x16x32_bf16 v[180:183], v[60:63], v[36:39], v[180:183]
	v_mfma_f32_16x16x32_bf16 v[184:187], v[60:63], v[40:43], v[184:187]
	v_mfma_f32_16x16x32_bf16 v[188:191], v[60:63], v[44:47], v[188:191]
	v_mfma_f32_16x16x32_bf16 v[192:195], v[64:67], v[32:35], v[192:195]
	v_mfma_f32_16x16x32_bf16 v[196:199], v[64:67], v[36:39], v[196:199]
	v_mfma_f32_16x16x32_bf16 v[200:203], v[64:67], v[40:43], v[200:203]
	v_mfma_f32_16x16x32_bf16 v[204:207], v[64:67], v[44:47], v[204:207]
	v_mfma_f32_16x16x32_bf16 v[208:211], v[68:71], v[32:35], v[208:211]
	v_mfma_f32_16x16x32_bf16 v[212:215], v[68:71], v[36:39], v[212:215]
	v_mfma_f32_16x16x32_bf16 v[216:219], v[68:71], v[40:43], v[216:219]
	v_mfma_f32_16x16x32_bf16 v[220:223], v[68:71], v[44:47], v[220:223]
	v_mfma_f32_16x16x32_bf16 v[224:227], v[72:75], v[32:35], v[224:227]
	v_mfma_f32_16x16x32_bf16 v[228:231], v[72:75], v[36:39], v[228:231]
	v_mfma_f32_16x16x32_bf16 v[232:235], v[72:75], v[40:43], v[232:235]
	v_mfma_f32_16x16x32_bf16 v[236:239], v[72:75], v[44:47], v[236:239]
	v_mfma_f32_16x16x32_bf16 v[240:243], v[76:79], v[32:35], v[240:243]
	v_mfma_f32_16x16x32_bf16 v[244:247], v[76:79], v[36:39], v[244:247]
	v_mfma_f32_16x16x32_bf16 v[248:251], v[76:79], v[40:43], v[248:251]
	v_mfma_f32_16x16x32_bf16 v[252:255], v[76:79], v[44:47], v[252:255]
	s_waitcnt lgkmcnt(0)
	v_mfma_f32_16x16x32_bf16 v[128:131], v[96:99], v[80:83], v[128:131]
	v_mfma_f32_16x16x32_bf16 v[132:135], v[96:99], v[84:87], v[132:135]
	global_load_dwordx4 v[32:35], v21, s[8:9] offset:0
	v_mfma_f32_16x16x32_bf16 v[136:139], v[96:99], v[88:91], v[136:139]
	v_mfma_f32_16x16x32_bf16 v[140:143], v[96:99], v[92:95], v[140:143]
	global_load_dwordx4 v[36:39], v21, s[8:9] offset:16
	v_mfma_f32_16x16x32_bf16 v[144:147], v[100:103], v[80:83], v[144:147]
	v_mfma_f32_16x16x32_bf16 v[148:151], v[100:103], v[84:87], v[148:151]
	global_load_dwordx4 v[40:43], v21, s[8:9] offset:32
	v_mfma_f32_16x16x32_bf16 v[152:155], v[100:103], v[88:91], v[152:155]
	v_mfma_f32_16x16x32_bf16 v[156:159], v[100:103], v[92:95], v[156:159]
	global_load_dwordx4 v[44:47], v21, s[8:9] offset:48
	v_mfma_f32_16x16x32_bf16 v[160:163], v[104:107], v[80:83], v[160:163]
	v_mfma_f32_16x16x32_bf16 v[164:167], v[104:107], v[84:87], v[164:167]
	global_load_dwordx4 v[48:51], v21, s[8:9] offset:1024
	v_mfma_f32_16x16x32_bf16 v[168:171], v[104:107], v[88:91], v[168:171]
	v_mfma_f32_16x16x32_bf16 v[172:175], v[104:107], v[92:95], v[172:175]
	global_load_dwordx4 v[52:55], v21, s[8:9] offset:1040
	v_mfma_f32_16x16x32_bf16 v[176:179], v[108:111], v[80:83], v[176:179]
	v_mfma_f32_16x16x32_bf16 v[180:183], v[108:111], v[84:87], v[180:183]
	global_load_dwordx4 v[56:59], v21, s[8:9] offset:1056
	v_mfma_f32_16x16x32_bf16 v[184:187], v[108:111], v[88:91], v[184:187]
	v_mfma_f32_16x16x32_bf16 v[188:191], v[108:111], v[92:95], v[188:191]
	global_load_dwordx4 v[60:63], v21, s[8:9] offset:1072
	v_mfma_f32_16x16x32_bf16 v[192:195], v[112:115], v[80:83], v[192:195]
	v_mfma_f32_16x16x32_bf16 v[196:199], v[112:115], v[84:87], v[196:199]
	global_load_dwordx4 v[64:67], v21, s[8:9] offset:2048
	v_mfma_f32_16x16x32_bf16 v[200:203], v[112:115], v[88:91], v[200:203]
	v_mfma_f32_16x16x32_bf16 v[204:207], v[112:115], v[92:95], v[204:207]
	global_load_dwordx4 v[68:71], v21, s[8:9] offset:2064
	v_mfma_f32_16x16x32_bf16 v[208:211], v[116:119], v[80:83], v[208:211]
	v_mfma_f32_16x16x32_bf16 v[212:215], v[116:119], v[84:87], v[212:215]
	global_load_dwordx4 v[72:75], v21, s[8:9] offset:2080
	v_mfma_f32_16x16x32_bf16 v[216:219], v[116:119], v[88:91], v[216:219]
	v_mfma_f32_16x16x32_bf16 v[220:223], v[116:119], v[92:95], v[220:223]
	global_load_dwordx4 v[76:79], v21, s[8:9] offset:2096
	v_mfma_f32_16x16x32_bf16 v[224:227], v[120:123], v[80:83], v[224:227]
	v_mfma_f32_16x16x32_bf16 v[228:231], v[120:123], v[84:87], v[228:231]
	v_mfma_f32_16x16x32_bf16 v[232:235], v[120:123], v[88:91], v[232:235]
	v_mfma_f32_16x16x32_bf16 v[236:239], v[120:123], v[92:95], v[236:239]
	v_mfma_f32_16x16x32_bf16 v[240:243], v[124:127], v[80:83], v[240:243]
	v_mfma_f32_16x16x32_bf16 v[244:247], v[124:127], v[84:87], v[244:247]
	v_mfma_f32_16x16x32_bf16 v[248:251], v[124:127], v[88:91], v[248:251]
	v_mfma_f32_16x16x32_bf16 v[252:255], v[124:127], v[92:95], v[252:255]
	global_load_dwordx4 v[80:83], v21, s[8:9] offset:3072
	global_load_dwordx4 v[84:87], v21, s[8:9] offset:3088
	global_load_dwordx4 v[88:91], v21, s[8:9] offset:3104
	global_load_dwordx4 v[92:95], v21, s[8:9] offset:3120
	v_mov_b32_e32 v31, 0x358637bd
	s_waitcnt vmcnt(0)
	v_add_f32_e32 v32, v32, v33
	v_add_f32_e32 v34, v34, v35
	v_add_f32_e32 v36, v36, v37
	v_add_f32_e32 v38, v38, v39
	v_add_f32_e32 v40, v40, v41
	v_add_f32_e32 v42, v42, v43
	v_add_f32_e32 v44, v44, v45
	v_add_f32_e32 v46, v46, v47
	v_add_f32_e32 v32, v32, v34
	v_add_f32_e32 v36, v36, v38
	v_add_f32_e32 v40, v40, v42
	v_add_f32_e32 v44, v44, v46
	v_add_f32_e32 v32, v32, v36
	v_add_f32_e32 v40, v40, v44
	v_add_f32_e32 v32, v32, v40
	v_add_f32_e32 v48, v48, v49
	v_add_f32_e32 v50, v50, v51
	v_add_f32_e32 v52, v52, v53
	v_add_f32_e32 v54, v54, v55
	v_add_f32_e32 v56, v56, v57
	v_add_f32_e32 v58, v58, v59
	v_add_f32_e32 v60, v60, v61
	v_add_f32_e32 v62, v62, v63
	v_add_f32_e32 v48, v48, v50
	v_add_f32_e32 v52, v52, v54
	v_add_f32_e32 v56, v56, v58
	v_add_f32_e32 v60, v60, v62
	v_add_f32_e32 v48, v48, v52
	v_add_f32_e32 v56, v56, v60
	v_add_f32_e32 v48, v48, v56
	v_add_f32_e32 v64, v64, v65
	v_add_f32_e32 v66, v66, v67
	v_add_f32_e32 v68, v68, v69
	v_add_f32_e32 v70, v70, v71
	v_add_f32_e32 v72, v72, v73
	v_add_f32_e32 v74, v74, v75
	v_add_f32_e32 v76, v76, v77
	v_add_f32_e32 v78, v78, v79
	v_add_f32_e32 v64, v64, v66
	v_add_f32_e32 v68, v68, v70
	v_add_f32_e32 v72, v72, v74
	v_add_f32_e32 v76, v76, v78
	v_add_f32_e32 v64, v64, v68
	v_add_f32_e32 v72, v72, v76
	v_add_f32_e32 v64, v64, v72
	v_add_f32_e32 v80, v80, v81
	v_add_f32_e32 v82, v82, v83
	v_add_f32_e32 v84, v84, v85
	v_add_f32_e32 v86, v86, v87
	v_add_f32_e32 v88, v88, v89
	v_add_f32_e32 v90, v90, v91
	v_add_f32_e32 v92, v92, v93
	v_add_f32_e32 v94, v94, v95
	v_add_f32_e32 v80, v80, v82
	v_add_f32_e32 v84, v84, v86
	v_add_f32_e32 v88, v88, v90
	v_add_f32_e32 v92, v92, v94
	v_add_f32_e32 v80, v80, v84
	v_add_f32_e32 v88, v88, v92
	v_add_f32_e32 v80, v80, v88
	v_fmamk_f32 v20, v32, 0x3aaaaaab, v31
	v_fmamk_f32 v22, v48, 0x3aaaaaab, v31
	v_fmamk_f32 v24, v64, 0x3aaaaaab, v31
	v_fmamk_f32 v26, v80, 0x3aaaaaab, v31
	v_rsq_f32_e32 v20, v20
	v_rsq_f32_e32 v22, v22
	v_rsq_f32_e32 v24, v24
	v_rsq_f32_e32 v26, v26
	s_nop 0
	v_bfe_u32 v28, v0, 4, 1
	v_mul_u32_u24_e32 v28, 24, v28
	v_add_u32_e32 v16, v16, v28
	v_add_u32_e32 v17, v17, v28
	v_add_u32_e32 v18, v18, v28
	v_add_u32_e32 v19, v19, v28
	v_pk_mul_f32 v[128:129], v[128:129], v[20:21] op_sel_hi:[1,0]
	v_pk_mul_f32 v[130:131], v[130:131], v[20:21] op_sel_hi:[1,0]
	v_pk_mul_f32 v[144:145], v[144:145], v[20:21] op_sel_hi:[1,0]
	v_pk_mul_f32 v[146:147], v[146:147], v[20:21] op_sel_hi:[1,0]
	v_pk_mul_f32 v[32:33], v[128:129], s[26:27]
	v_pk_mul_f32 v[34:35], v[130:131], s[26:27]
	v_pk_mul_f32 v[36:37], v[144:145], s[26:27]
	v_pk_mul_f32 v[38:39], v[146:147], s[26:27]
	v_pk_fma_f32 v[32:33], v[128:129], v[32:33], s[28:29] neg_lo:[1,0,0] neg_hi:[1,0,0]
	v_pk_fma_f32 v[34:35], v[130:131], v[34:35], s[28:29] neg_lo:[1,0,0] neg_hi:[1,0,0]
	v_pk_fma_f32 v[36:37], v[144:145], v[36:37], s[28:29] neg_lo:[1,0,0] neg_hi:[1,0,0]
	v_pk_fma_f32 v[38:39], v[146:147], v[38:39], s[28:29] neg_lo:[1,0,0] neg_hi:[1,0,0]
	v_pk_mul_f32 v[32:33], v[128:129], v[32:33]
	v_pk_mul_f32 v[34:35], v[130:131], v[34:35]
	v_pk_mul_f32 v[36:37], v[144:145], v[36:37]
	v_pk_mul_f32 v[38:39], v[146:147], v[38:39]
	v_exp_f32_e32 v32, v32
	v_exp_f32_e32 v33, v33
	v_exp_f32_e32 v34, v34
	v_exp_f32_e32 v35, v35
	v_exp_f32_e32 v36, v36
	v_exp_f32_e32 v37, v37
	v_exp_f32_e32 v38, v38
	v_exp_f32_e32 v39, v39
	v_pk_add_f32 v[32:33], v[32:33], s[30:31]
	v_pk_add_f32 v[34:35], v[34:35], s[30:31]
	v_pk_add_f32 v[36:37], v[36:37], s[30:31]
	v_pk_add_f32 v[38:39], v[38:39], s[30:31]
	v_rcp_f32_e32 v32, v32
	v_rcp_f32_e32 v33, v33
	v_rcp_f32_e32 v34, v34
	v_rcp_f32_e32 v35, v35
	v_rcp_f32_e32 v36, v36
	v_rcp_f32_e32 v37, v37
	v_rcp_f32_e32 v38, v38
	v_rcp_f32_e32 v39, v39
	s_nop 0
	v_pk_mul_f32 v[128:129], v[128:129], v[32:33]
	v_pk_mul_f32 v[130:131], v[130:131], v[34:35]
	v_pk_mul_f32 v[144:145], v[144:145], v[36:37]
	v_pk_mul_f32 v[146:147], v[146:147], v[38:39]
	v_cvt_pk_bf16_f32 v64, v128, v129
	v_cvt_pk_bf16_f32 v65, v130, v131
	v_cvt_pk_bf16_f32 v66, v144, v145
	v_cvt_pk_bf16_f32 v67, v146, v147
	s_nop 1
	v_permlane16_swap_b32 v64, v66
	v_permlane16_swap_b32 v65, v67
	global_store_dwordx4 v16, v[64:67], s[10:11]
	v_pk_mul_f32 v[160:161], v[160:161], v[20:21] op_sel_hi:[1,0]
	v_pk_mul_f32 v[162:163], v[162:163], v[20:21] op_sel_hi:[1,0]
	v_pk_mul_f32 v[176:177], v[176:177], v[20:21] op_sel_hi:[1,0]
	v_pk_mul_f32 v[178:179], v[178:179], v[20:21] op_sel_hi:[1,0]
	v_pk_mul_f32 v[48:49], v[160:161], s[26:27]
	v_pk_mul_f32 v[50:51], v[162:163], s[26:27]
	v_pk_mul_f32 v[52:53], v[176:177], s[26:27]
	v_pk_mul_f32 v[54:55], v[178:179], s[26:27]
	v_pk_fma_f32 v[48:49], v[160:161], v[48:49], s[28:29] neg_lo:[1,0,0] neg_hi:[1,0,0]
	v_pk_fma_f32 v[50:51], v[162:163], v[50:51], s[28:29] neg_lo:[1,0,0] neg_hi:[1,0,0]
	v_pk_fma_f32 v[52:53], v[176:177], v[52:53], s[28:29] neg_lo:[1,0,0] neg_hi:[1,0,0]
	v_pk_fma_f32 v[54:55], v[178:179], v[54:55], s[28:29] neg_lo:[1,0,0] neg_hi:[1,0,0]
	v_pk_mul_f32 v[48:49], v[160:161], v[48:49]
	v_pk_mul_f32 v[50:51], v[162:163], v[50:51]
	v_pk_mul_f32 v[52:53], v[176:177], v[52:53]
	v_pk_mul_f32 v[54:55], v[178:179], v[54:55]
	v_exp_f32_e32 v48, v48
	v_exp_f32_e32 v49, v49
	v_exp_f32_e32 v50, v50
	v_exp_f32_e32 v51, v51
	v_exp_f32_e32 v52, v52
	v_exp_f32_e32 v53, v53
	v_exp_f32_e32 v54, v54
	v_exp_f32_e32 v55, v55
	v_pk_add_f32 v[48:49], v[48:49], s[30:31]
	v_pk_add_f32 v[50:51], v[50:51], s[30:31]
	v_pk_add_f32 v[52:53], v[52:53], s[30:31]
	v_pk_add_f32 v[54:55], v[54:55], s[30:31]
	v_rcp_f32_e32 v48, v48
	v_rcp_f32_e32 v49, v49
	v_rcp_f32_e32 v50, v50
	v_rcp_f32_e32 v51, v51
	v_rcp_f32_e32 v52, v52
	v_rcp_f32_e32 v53, v53
	v_rcp_f32_e32 v54, v54
	v_rcp_f32_e32 v55, v55
	s_nop 0
	v_pk_mul_f32 v[160:161], v[160:161], v[48:49]
	v_pk_mul_f32 v[162:163], v[162:163], v[50:51]
	v_pk_mul_f32 v[176:177], v[176:177], v[52:53]
	v_pk_mul_f32 v[178:179], v[178:179], v[54:55]
	v_cvt_pk_bf16_f32 v68, v160, v161
	v_cvt_pk_bf16_f32 v69, v162, v163
	v_cvt_pk_bf16_f32 v70, v176, v177
	v_cvt_pk_bf16_f32 v71, v178, v179
	s_nop 1
	v_permlane16_swap_b32 v68, v70
	v_permlane16_swap_b32 v69, v71
	global_store_dwordx4 v16, v[68:71], s[10:11] offset:64
	v_pk_mul_f32 v[192:193], v[192:193], v[20:21] op_sel_hi:[1,0]
	v_pk_mul_f32 v[194:195], v[194:195], v[20:21] op_sel_hi:[1,0]
	v_pk_mul_f32 v[208:209], v[208:209], v[20:21] op_sel_hi:[1,0]
	v_pk_mul_f32 v[210:211], v[210:211], v[20:21] op_sel_hi:[1,0]
	v_pk_mul_f32 v[32:33], v[192:193], s[26:27]
	v_pk_mul_f32 v[34:35], v[194:195], s[26:27]
	v_pk_mul_f32 v[36:37], v[208:209], s[26:27]
	v_pk_mul_f32 v[38:39], v[210:211], s[26:27]
	v_pk_fma_f32 v[32:33], v[192:193], v[32:33], s[28:29] neg_lo:[1,0,0] neg_hi:[1,0,0]
	v_pk_fma_f32 v[34:35], v[194:195], v[34:35], s[28:29] neg_lo:[1,0,0] neg_hi:[1,0,0]
	v_pk_fma_f32 v[36:37], v[208:209], v[36:37], s[28:29] neg_lo:[1,0,0] neg_hi:[1,0,0]
	v_pk_fma_f32 v[38:39], v[210:211], v[38:39], s[28:29] neg_lo:[1,0,0] neg_hi:[1,0,0]
	v_pk_mul_f32 v[32:33], v[192:193], v[32:33]
	v_pk_mul_f32 v[34:35], v[194:195], v[34:35]
	v_pk_mul_f32 v[36:37], v[208:209], v[36:37]
	v_pk_mul_f32 v[38:39], v[210:211], v[38:39]
	v_exp_f32_e32 v32, v32
	v_exp_f32_e32 v33, v33
	v_exp_f32_e32 v34, v34
	v_exp_f32_e32 v35, v35
	v_exp_f32_e32 v36, v36
	v_exp_f32_e32 v37, v37
	v_exp_f32_e32 v38, v38
	v_exp_f32_e32 v39, v39
	v_pk_add_f32 v[32:33], v[32:33], s[30:31]
	v_pk_add_f32 v[34:35], v[34:35], s[30:31]
	v_pk_add_f32 v[36:37], v[36:37], s[30:31]
	v_pk_add_f32 v[38:39], v[38:39], s[30:31]
	v_rcp_f32_e32 v32, v32
	v_rcp_f32_e32 v33, v33
	v_rcp_f32_e32 v34, v34
	v_rcp_f32_e32 v35, v35
	v_rcp_f32_e32 v36, v36
	v_rcp_f32_e32 v37, v37
	v_rcp_f32_e32 v38, v38
	v_rcp_f32_e32 v39, v39
	s_nop 0
	v_pk_mul_f32 v[192:193], v[192:193], v[32:33]
	v_pk_mul_f32 v[194:195], v[194:195], v[34:35]
	v_pk_mul_f32 v[208:209], v[208:209], v[36:37]
	v_pk_mul_f32 v[210:211], v[210:211], v[38:39]
	v_cvt_pk_bf16_f32 v64, v192, v193
	v_cvt_pk_bf16_f32 v65, v194, v195
	v_cvt_pk_bf16_f32 v66, v208, v209
	v_cvt_pk_bf16_f32 v67, v210, v211
	s_nop 1
	v_permlane16_swap_b32 v64, v66
	v_permlane16_swap_b32 v65, v67
	global_store_dwordx4 v16, v[64:67], s[10:11] offset:128
	v_pk_mul_f32 v[224:225], v[224:225], v[20:21] op_sel_hi:[1,0]
	v_pk_mul_f32 v[226:227], v[226:227], v[20:21] op_sel_hi:[1,0]
	v_pk_mul_f32 v[240:241], v[240:241], v[20:21] op_sel_hi:[1,0]
	v_pk_mul_f32 v[242:243], v[242:243], v[20:21] op_sel_hi:[1,0]
	v_pk_mul_f32 v[48:49], v[224:225], s[26:27]
	v_pk_mul_f32 v[50:51], v[226:227], s[26:27]
	v_pk_mul_f32 v[52:53], v[240:241], s[26:27]
	v_pk_mul_f32 v[54:55], v[242:243], s[26:27]
	v_pk_fma_f32 v[48:49], v[224:225], v[48:49], s[28:29] neg_lo:[1,0,0] neg_hi:[1,0,0]
	v_pk_fma_f32 v[50:51], v[226:227], v[50:51], s[28:29] neg_lo:[1,0,0] neg_hi:[1,0,0]
	v_pk_fma_f32 v[52:53], v[240:241], v[52:53], s[28:29] neg_lo:[1,0,0] neg_hi:[1,0,0]
	v_pk_fma_f32 v[54:55], v[242:243], v[54:55], s[28:29] neg_lo:[1,0,0] neg_hi:[1,0,0]
	v_pk_mul_f32 v[48:49], v[224:225], v[48:49]
	v_pk_mul_f32 v[50:51], v[226:227], v[50:51]
	v_pk_mul_f32 v[52:53], v[240:241], v[52:53]
	v_pk_mul_f32 v[54:55], v[242:243], v[54:55]
	v_exp_f32_e32 v48, v48
	v_exp_f32_e32 v49, v49
	v_exp_f32_e32 v50, v50
	v_exp_f32_e32 v51, v51
	v_exp_f32_e32 v52, v52
	v_exp_f32_e32 v53, v53
	v_exp_f32_e32 v54, v54
	v_exp_f32_e32 v55, v55
	v_pk_add_f32 v[48:49], v[48:49], s[30:31]
	v_pk_add_f32 v[50:51], v[50:51], s[30:31]
	v_pk_add_f32 v[52:53], v[52:53], s[30:31]
	v_pk_add_f32 v[54:55], v[54:55], s[30:31]
	v_rcp_f32_e32 v48, v48
	v_rcp_f32_e32 v49, v49
	v_rcp_f32_e32 v50, v50
	v_rcp_f32_e32 v51, v51
	v_rcp_f32_e32 v52, v52
	v_rcp_f32_e32 v53, v53
	v_rcp_f32_e32 v54, v54
	v_rcp_f32_e32 v55, v55
	s_nop 0
	v_pk_mul_f32 v[224:225], v[224:225], v[48:49]
	v_pk_mul_f32 v[226:227], v[226:227], v[50:51]
	v_pk_mul_f32 v[240:241], v[240:241], v[52:53]
	v_pk_mul_f32 v[242:243], v[242:243], v[54:55]
	v_cvt_pk_bf16_f32 v68, v224, v225
	v_cvt_pk_bf16_f32 v69, v226, v227
	v_cvt_pk_bf16_f32 v70, v240, v241
	v_cvt_pk_bf16_f32 v71, v242, v243
	s_nop 1
	v_permlane16_swap_b32 v68, v70
	v_permlane16_swap_b32 v69, v71
	global_store_dwordx4 v16, v[68:71], s[10:11] offset:192
	v_pk_mul_f32 v[132:133], v[132:133], v[22:23] op_sel_hi:[1,0]
	v_pk_mul_f32 v[134:135], v[134:135], v[22:23] op_sel_hi:[1,0]
	v_pk_mul_f32 v[148:149], v[148:149], v[22:23] op_sel_hi:[1,0]
	v_pk_mul_f32 v[150:151], v[150:151], v[22:23] op_sel_hi:[1,0]
	v_pk_mul_f32 v[32:33], v[132:133], s[26:27]
	v_pk_mul_f32 v[34:35], v[134:135], s[26:27]
	v_pk_mul_f32 v[36:37], v[148:149], s[26:27]
	v_pk_mul_f32 v[38:39], v[150:151], s[26:27]
	v_pk_fma_f32 v[32:33], v[132:133], v[32:33], s[28:29] neg_lo:[1,0,0] neg_hi:[1,0,0]
	v_pk_fma_f32 v[34:35], v[134:135], v[34:35], s[28:29] neg_lo:[1,0,0] neg_hi:[1,0,0]
	v_pk_fma_f32 v[36:37], v[148:149], v[36:37], s[28:29] neg_lo:[1,0,0] neg_hi:[1,0,0]
	v_pk_fma_f32 v[38:39], v[150:151], v[38:39], s[28:29] neg_lo:[1,0,0] neg_hi:[1,0,0]
	v_pk_mul_f32 v[32:33], v[132:133], v[32:33]
	v_pk_mul_f32 v[34:35], v[134:135], v[34:35]
	v_pk_mul_f32 v[36:37], v[148:149], v[36:37]
	v_pk_mul_f32 v[38:39], v[150:151], v[38:39]
	v_exp_f32_e32 v32, v32
	v_exp_f32_e32 v33, v33
	v_exp_f32_e32 v34, v34
	v_exp_f32_e32 v35, v35
	v_exp_f32_e32 v36, v36
	v_exp_f32_e32 v37, v37
	v_exp_f32_e32 v38, v38
	v_exp_f32_e32 v39, v39
	v_pk_add_f32 v[32:33], v[32:33], s[30:31]
	v_pk_add_f32 v[34:35], v[34:35], s[30:31]
	v_pk_add_f32 v[36:37], v[36:37], s[30:31]
	v_pk_add_f32 v[38:39], v[38:39], s[30:31]
	v_rcp_f32_e32 v32, v32
	v_rcp_f32_e32 v33, v33
	v_rcp_f32_e32 v34, v34
	v_rcp_f32_e32 v35, v35
	v_rcp_f32_e32 v36, v36
	v_rcp_f32_e32 v37, v37
	v_rcp_f32_e32 v38, v38
	v_rcp_f32_e32 v39, v39
	s_nop 0
	v_pk_mul_f32 v[132:133], v[132:133], v[32:33]
	v_pk_mul_f32 v[134:135], v[134:135], v[34:35]
	v_pk_mul_f32 v[148:149], v[148:149], v[36:37]
	v_pk_mul_f32 v[150:151], v[150:151], v[38:39]
	v_cvt_pk_bf16_f32 v64, v132, v133
	v_cvt_pk_bf16_f32 v65, v134, v135
	v_cvt_pk_bf16_f32 v66, v148, v149
	v_cvt_pk_bf16_f32 v67, v150, v151
	s_nop 1
	v_permlane16_swap_b32 v64, v66
	v_permlane16_swap_b32 v65, v67
	global_store_dwordx4 v17, v[64:67], s[10:11]
	v_pk_mul_f32 v[164:165], v[164:165], v[22:23] op_sel_hi:[1,0]
	v_pk_mul_f32 v[166:167], v[166:167], v[22:23] op_sel_hi:[1,0]
	v_pk_mul_f32 v[180:181], v[180:181], v[22:23] op_sel_hi:[1,0]
	v_pk_mul_f32 v[182:183], v[182:183], v[22:23] op_sel_hi:[1,0]
	v_pk_mul_f32 v[48:49], v[164:165], s[26:27]
	v_pk_mul_f32 v[50:51], v[166:167], s[26:27]
	v_pk_mul_f32 v[52:53], v[180:181], s[26:27]
	v_pk_mul_f32 v[54:55], v[182:183], s[26:27]
	v_pk_fma_f32 v[48:49], v[164:165], v[48:49], s[28:29] neg_lo:[1,0,0] neg_hi:[1,0,0]
	v_pk_fma_f32 v[50:51], v[166:167], v[50:51], s[28:29] neg_lo:[1,0,0] neg_hi:[1,0,0]
	v_pk_fma_f32 v[52:53], v[180:181], v[52:53], s[28:29] neg_lo:[1,0,0] neg_hi:[1,0,0]
	v_pk_fma_f32 v[54:55], v[182:183], v[54:55], s[28:29] neg_lo:[1,0,0] neg_hi:[1,0,0]
	v_pk_mul_f32 v[48:49], v[164:165], v[48:49]
	v_pk_mul_f32 v[50:51], v[166:167], v[50:51]
	v_pk_mul_f32 v[52:53], v[180:181], v[52:53]
	v_pk_mul_f32 v[54:55], v[182:183], v[54:55]
	v_exp_f32_e32 v48, v48
	v_exp_f32_e32 v49, v49
	v_exp_f32_e32 v50, v50
	v_exp_f32_e32 v51, v51
	v_exp_f32_e32 v52, v52
	v_exp_f32_e32 v53, v53
	v_exp_f32_e32 v54, v54
	v_exp_f32_e32 v55, v55
	v_pk_add_f32 v[48:49], v[48:49], s[30:31]
	v_pk_add_f32 v[50:51], v[50:51], s[30:31]
	v_pk_add_f32 v[52:53], v[52:53], s[30:31]
	v_pk_add_f32 v[54:55], v[54:55], s[30:31]
	v_rcp_f32_e32 v48, v48
	v_rcp_f32_e32 v49, v49
	v_rcp_f32_e32 v50, v50
	v_rcp_f32_e32 v51, v51
	v_rcp_f32_e32 v52, v52
	v_rcp_f32_e32 v53, v53
	v_rcp_f32_e32 v54, v54
	v_rcp_f32_e32 v55, v55
	s_nop 0
	v_pk_mul_f32 v[164:165], v[164:165], v[48:49]
	v_pk_mul_f32 v[166:167], v[166:167], v[50:51]
	v_pk_mul_f32 v[180:181], v[180:181], v[52:53]
	v_pk_mul_f32 v[182:183], v[182:183], v[54:55]
	v_cvt_pk_bf16_f32 v68, v164, v165
	v_cvt_pk_bf16_f32 v69, v166, v167
	v_cvt_pk_bf16_f32 v70, v180, v181
	v_cvt_pk_bf16_f32 v71, v182, v183
	s_nop 1
	v_permlane16_swap_b32 v68, v70
	v_permlane16_swap_b32 v69, v71
	global_store_dwordx4 v17, v[68:71], s[10:11] offset:64
	v_pk_mul_f32 v[196:197], v[196:197], v[22:23] op_sel_hi:[1,0]
	v_pk_mul_f32 v[198:199], v[198:199], v[22:23] op_sel_hi:[1,0]
	v_pk_mul_f32 v[212:213], v[212:213], v[22:23] op_sel_hi:[1,0]
	v_pk_mul_f32 v[214:215], v[214:215], v[22:23] op_sel_hi:[1,0]
	v_pk_mul_f32 v[32:33], v[196:197], s[26:27]
	v_pk_mul_f32 v[34:35], v[198:199], s[26:27]
	v_pk_mul_f32 v[36:37], v[212:213], s[26:27]
	v_pk_mul_f32 v[38:39], v[214:215], s[26:27]
	v_pk_fma_f32 v[32:33], v[196:197], v[32:33], s[28:29] neg_lo:[1,0,0] neg_hi:[1,0,0]
	v_pk_fma_f32 v[34:35], v[198:199], v[34:35], s[28:29] neg_lo:[1,0,0] neg_hi:[1,0,0]
	v_pk_fma_f32 v[36:37], v[212:213], v[36:37], s[28:29] neg_lo:[1,0,0] neg_hi:[1,0,0]
	v_pk_fma_f32 v[38:39], v[214:215], v[38:39], s[28:29] neg_lo:[1,0,0] neg_hi:[1,0,0]
	v_pk_mul_f32 v[32:33], v[196:197], v[32:33]
	v_pk_mul_f32 v[34:35], v[198:199], v[34:35]
	v_pk_mul_f32 v[36:37], v[212:213], v[36:37]
	v_pk_mul_f32 v[38:39], v[214:215], v[38:39]
	v_exp_f32_e32 v32, v32
	v_exp_f32_e32 v33, v33
	v_exp_f32_e32 v34, v34
	v_exp_f32_e32 v35, v35
	v_exp_f32_e32 v36, v36
	v_exp_f32_e32 v37, v37
	v_exp_f32_e32 v38, v38
	v_exp_f32_e32 v39, v39
	v_pk_add_f32 v[32:33], v[32:33], s[30:31]
	v_pk_add_f32 v[34:35], v[34:35], s[30:31]
	v_pk_add_f32 v[36:37], v[36:37], s[30:31]
	v_pk_add_f32 v[38:39], v[38:39], s[30:31]
	v_rcp_f32_e32 v32, v32
	v_rcp_f32_e32 v33, v33
	v_rcp_f32_e32 v34, v34
	v_rcp_f32_e32 v35, v35
	v_rcp_f32_e32 v36, v36
	v_rcp_f32_e32 v37, v37
	v_rcp_f32_e32 v38, v38
	v_rcp_f32_e32 v39, v39
	s_nop 0
	v_pk_mul_f32 v[196:197], v[196:197], v[32:33]
	v_pk_mul_f32 v[198:199], v[198:199], v[34:35]
	v_pk_mul_f32 v[212:213], v[212:213], v[36:37]
	v_pk_mul_f32 v[214:215], v[214:215], v[38:39]
	v_cvt_pk_bf16_f32 v64, v196, v197
	v_cvt_pk_bf16_f32 v65, v198, v199
	v_cvt_pk_bf16_f32 v66, v212, v213
	v_cvt_pk_bf16_f32 v67, v214, v215
	s_nop 1
	v_permlane16_swap_b32 v64, v66
	v_permlane16_swap_b32 v65, v67
	global_store_dwordx4 v17, v[64:67], s[10:11] offset:128
	v_pk_mul_f32 v[228:229], v[228:229], v[22:23] op_sel_hi:[1,0]
	v_pk_mul_f32 v[230:231], v[230:231], v[22:23] op_sel_hi:[1,0]
	v_pk_mul_f32 v[244:245], v[244:245], v[22:23] op_sel_hi:[1,0]
	v_pk_mul_f32 v[246:247], v[246:247], v[22:23] op_sel_hi:[1,0]
	v_pk_mul_f32 v[48:49], v[228:229], s[26:27]
	v_pk_mul_f32 v[50:51], v[230:231], s[26:27]
	v_pk_mul_f32 v[52:53], v[244:245], s[26:27]
	v_pk_mul_f32 v[54:55], v[246:247], s[26:27]
	v_pk_fma_f32 v[48:49], v[228:229], v[48:49], s[28:29] neg_lo:[1,0,0] neg_hi:[1,0,0]
	v_pk_fma_f32 v[50:51], v[230:231], v[50:51], s[28:29] neg_lo:[1,0,0] neg_hi:[1,0,0]
	v_pk_fma_f32 v[52:53], v[244:245], v[52:53], s[28:29] neg_lo:[1,0,0] neg_hi:[1,0,0]
	v_pk_fma_f32 v[54:55], v[246:247], v[54:55], s[28:29] neg_lo:[1,0,0] neg_hi:[1,0,0]
	v_pk_mul_f32 v[48:49], v[228:229], v[48:49]
	v_pk_mul_f32 v[50:51], v[230:231], v[50:51]
	v_pk_mul_f32 v[52:53], v[244:245], v[52:53]
	v_pk_mul_f32 v[54:55], v[246:247], v[54:55]
	v_exp_f32_e32 v48, v48
	v_exp_f32_e32 v49, v49
	v_exp_f32_e32 v50, v50
	v_exp_f32_e32 v51, v51
	v_exp_f32_e32 v52, v52
	v_exp_f32_e32 v53, v53
	v_exp_f32_e32 v54, v54
	v_exp_f32_e32 v55, v55
	v_pk_add_f32 v[48:49], v[48:49], s[30:31]
	v_pk_add_f32 v[50:51], v[50:51], s[30:31]
	v_pk_add_f32 v[52:53], v[52:53], s[30:31]
	v_pk_add_f32 v[54:55], v[54:55], s[30:31]
	v_rcp_f32_e32 v48, v48
	v_rcp_f32_e32 v49, v49
	v_rcp_f32_e32 v50, v50
	v_rcp_f32_e32 v51, v51
	v_rcp_f32_e32 v52, v52
	v_rcp_f32_e32 v53, v53
	v_rcp_f32_e32 v54, v54
	v_rcp_f32_e32 v55, v55
	s_nop 0
	v_pk_mul_f32 v[228:229], v[228:229], v[48:49]
	v_pk_mul_f32 v[230:231], v[230:231], v[50:51]
	v_pk_mul_f32 v[244:245], v[244:245], v[52:53]
	v_pk_mul_f32 v[246:247], v[246:247], v[54:55]
	v_cvt_pk_bf16_f32 v68, v228, v229
	v_cvt_pk_bf16_f32 v69, v230, v231
	v_cvt_pk_bf16_f32 v70, v244, v245
	v_cvt_pk_bf16_f32 v71, v246, v247
	s_nop 1
	v_permlane16_swap_b32 v68, v70
	v_permlane16_swap_b32 v69, v71
	global_store_dwordx4 v17, v[68:71], s[10:11] offset:192
	v_pk_mul_f32 v[136:137], v[136:137], v[24:25] op_sel_hi:[1,0]
	v_pk_mul_f32 v[138:139], v[138:139], v[24:25] op_sel_hi:[1,0]
	v_pk_mul_f32 v[152:153], v[152:153], v[24:25] op_sel_hi:[1,0]
	v_pk_mul_f32 v[154:155], v[154:155], v[24:25] op_sel_hi:[1,0]
	v_pk_mul_f32 v[32:33], v[136:137], s[26:27]
	v_pk_mul_f32 v[34:35], v[138:139], s[26:27]
	v_pk_mul_f32 v[36:37], v[152:153], s[26:27]
	v_pk_mul_f32 v[38:39], v[154:155], s[26:27]
	v_pk_fma_f32 v[32:33], v[136:137], v[32:33], s[28:29] neg_lo:[1,0,0] neg_hi:[1,0,0]
	v_pk_fma_f32 v[34:35], v[138:139], v[34:35], s[28:29] neg_lo:[1,0,0] neg_hi:[1,0,0]
	v_pk_fma_f32 v[36:37], v[152:153], v[36:37], s[28:29] neg_lo:[1,0,0] neg_hi:[1,0,0]
	v_pk_fma_f32 v[38:39], v[154:155], v[38:39], s[28:29] neg_lo:[1,0,0] neg_hi:[1,0,0]
	v_pk_mul_f32 v[32:33], v[136:137], v[32:33]
	v_pk_mul_f32 v[34:35], v[138:139], v[34:35]
	v_pk_mul_f32 v[36:37], v[152:153], v[36:37]
	v_pk_mul_f32 v[38:39], v[154:155], v[38:39]
	v_exp_f32_e32 v32, v32
	v_exp_f32_e32 v33, v33
	v_exp_f32_e32 v34, v34
	v_exp_f32_e32 v35, v35
	v_exp_f32_e32 v36, v36
	v_exp_f32_e32 v37, v37
	v_exp_f32_e32 v38, v38
	v_exp_f32_e32 v39, v39
	v_pk_add_f32 v[32:33], v[32:33], s[30:31]
	v_pk_add_f32 v[34:35], v[34:35], s[30:31]
	v_pk_add_f32 v[36:37], v[36:37], s[30:31]
	v_pk_add_f32 v[38:39], v[38:39], s[30:31]
	v_rcp_f32_e32 v32, v32
	v_rcp_f32_e32 v33, v33
	v_rcp_f32_e32 v34, v34
	v_rcp_f32_e32 v35, v35
	v_rcp_f32_e32 v36, v36
	v_rcp_f32_e32 v37, v37
	v_rcp_f32_e32 v38, v38
	v_rcp_f32_e32 v39, v39
	s_nop 0
	v_pk_mul_f32 v[136:137], v[136:137], v[32:33]
	v_pk_mul_f32 v[138:139], v[138:139], v[34:35]
	v_pk_mul_f32 v[152:153], v[152:153], v[36:37]
	v_pk_mul_f32 v[154:155], v[154:155], v[38:39]
	v_cvt_pk_bf16_f32 v64, v136, v137
	v_cvt_pk_bf16_f32 v65, v138, v139
	v_cvt_pk_bf16_f32 v66, v152, v153
	v_cvt_pk_bf16_f32 v67, v154, v155
	s_nop 1
	v_permlane16_swap_b32 v64, v66
	v_permlane16_swap_b32 v65, v67
	global_store_dwordx4 v18, v[64:67], s[10:11]
	v_pk_mul_f32 v[168:169], v[168:169], v[24:25] op_sel_hi:[1,0]
	v_pk_mul_f32 v[170:171], v[170:171], v[24:25] op_sel_hi:[1,0]
	v_pk_mul_f32 v[184:185], v[184:185], v[24:25] op_sel_hi:[1,0]
	v_pk_mul_f32 v[186:187], v[186:187], v[24:25] op_sel_hi:[1,0]
	v_pk_mul_f32 v[48:49], v[168:169], s[26:27]
	v_pk_mul_f32 v[50:51], v[170:171], s[26:27]
	v_pk_mul_f32 v[52:53], v[184:185], s[26:27]
	v_pk_mul_f32 v[54:55], v[186:187], s[26:27]
	v_pk_fma_f32 v[48:49], v[168:169], v[48:49], s[28:29] neg_lo:[1,0,0] neg_hi:[1,0,0]
	v_pk_fma_f32 v[50:51], v[170:171], v[50:51], s[28:29] neg_lo:[1,0,0] neg_hi:[1,0,0]
	v_pk_fma_f32 v[52:53], v[184:185], v[52:53], s[28:29] neg_lo:[1,0,0] neg_hi:[1,0,0]
	v_pk_fma_f32 v[54:55], v[186:187], v[54:55], s[28:29] neg_lo:[1,0,0] neg_hi:[1,0,0]
	v_pk_mul_f32 v[48:49], v[168:169], v[48:49]
	v_pk_mul_f32 v[50:51], v[170:171], v[50:51]
	v_pk_mul_f32 v[52:53], v[184:185], v[52:53]
	v_pk_mul_f32 v[54:55], v[186:187], v[54:55]
	v_exp_f32_e32 v48, v48
	v_exp_f32_e32 v49, v49
	v_exp_f32_e32 v50, v50
	v_exp_f32_e32 v51, v51
	v_exp_f32_e32 v52, v52
	v_exp_f32_e32 v53, v53
	v_exp_f32_e32 v54, v54
	v_exp_f32_e32 v55, v55
	v_pk_add_f32 v[48:49], v[48:49], s[30:31]
	v_pk_add_f32 v[50:51], v[50:51], s[30:31]
	v_pk_add_f32 v[52:53], v[52:53], s[30:31]
	v_pk_add_f32 v[54:55], v[54:55], s[30:31]
	v_rcp_f32_e32 v48, v48
	v_rcp_f32_e32 v49, v49
	v_rcp_f32_e32 v50, v50
	v_rcp_f32_e32 v51, v51
	v_rcp_f32_e32 v52, v52
	v_rcp_f32_e32 v53, v53
	v_rcp_f32_e32 v54, v54
	v_rcp_f32_e32 v55, v55
	s_nop 0
	v_pk_mul_f32 v[168:169], v[168:169], v[48:49]
	v_pk_mul_f32 v[170:171], v[170:171], v[50:51]
	v_pk_mul_f32 v[184:185], v[184:185], v[52:53]
	v_pk_mul_f32 v[186:187], v[186:187], v[54:55]
	v_cvt_pk_bf16_f32 v68, v168, v169
	v_cvt_pk_bf16_f32 v69, v170, v171
	v_cvt_pk_bf16_f32 v70, v184, v185
	v_cvt_pk_bf16_f32 v71, v186, v187
	s_nop 1
	v_permlane16_swap_b32 v68, v70
	v_permlane16_swap_b32 v69, v71
	global_store_dwordx4 v18, v[68:71], s[10:11] offset:64
	v_pk_mul_f32 v[200:201], v[200:201], v[24:25] op_sel_hi:[1,0]
	v_pk_mul_f32 v[202:203], v[202:203], v[24:25] op_sel_hi:[1,0]
	v_pk_mul_f32 v[216:217], v[216:217], v[24:25] op_sel_hi:[1,0]
	v_pk_mul_f32 v[218:219], v[218:219], v[24:25] op_sel_hi:[1,0]
	v_pk_mul_f32 v[32:33], v[200:201], s[26:27]
	v_pk_mul_f32 v[34:35], v[202:203], s[26:27]
	v_pk_mul_f32 v[36:37], v[216:217], s[26:27]
	v_pk_mul_f32 v[38:39], v[218:219], s[26:27]
	v_pk_fma_f32 v[32:33], v[200:201], v[32:33], s[28:29] neg_lo:[1,0,0] neg_hi:[1,0,0]
	v_pk_fma_f32 v[34:35], v[202:203], v[34:35], s[28:29] neg_lo:[1,0,0] neg_hi:[1,0,0]
	v_pk_fma_f32 v[36:37], v[216:217], v[36:37], s[28:29] neg_lo:[1,0,0] neg_hi:[1,0,0]
	v_pk_fma_f32 v[38:39], v[218:219], v[38:39], s[28:29] neg_lo:[1,0,0] neg_hi:[1,0,0]
	v_pk_mul_f32 v[32:33], v[200:201], v[32:33]
	v_pk_mul_f32 v[34:35], v[202:203], v[34:35]
	v_pk_mul_f32 v[36:37], v[216:217], v[36:37]
	v_pk_mul_f32 v[38:39], v[218:219], v[38:39]
	v_exp_f32_e32 v32, v32
	v_exp_f32_e32 v33, v33
	v_exp_f32_e32 v34, v34
	v_exp_f32_e32 v35, v35
	v_exp_f32_e32 v36, v36
	v_exp_f32_e32 v37, v37
	v_exp_f32_e32 v38, v38
	v_exp_f32_e32 v39, v39
	v_pk_add_f32 v[32:33], v[32:33], s[30:31]
	v_pk_add_f32 v[34:35], v[34:35], s[30:31]
	v_pk_add_f32 v[36:37], v[36:37], s[30:31]
	v_pk_add_f32 v[38:39], v[38:39], s[30:31]
	v_rcp_f32_e32 v32, v32
	v_rcp_f32_e32 v33, v33
	v_rcp_f32_e32 v34, v34
	v_rcp_f32_e32 v35, v35
	v_rcp_f32_e32 v36, v36
	v_rcp_f32_e32 v37, v37
	v_rcp_f32_e32 v38, v38
	v_rcp_f32_e32 v39, v39
	s_nop 0
	v_pk_mul_f32 v[200:201], v[200:201], v[32:33]
	v_pk_mul_f32 v[202:203], v[202:203], v[34:35]
	v_pk_mul_f32 v[216:217], v[216:217], v[36:37]
	v_pk_mul_f32 v[218:219], v[218:219], v[38:39]
	v_cvt_pk_bf16_f32 v64, v200, v201
	v_cvt_pk_bf16_f32 v65, v202, v203
	v_cvt_pk_bf16_f32 v66, v216, v217
	v_cvt_pk_bf16_f32 v67, v218, v219
	s_nop 1
	v_permlane16_swap_b32 v64, v66
	v_permlane16_swap_b32 v65, v67
	global_store_dwordx4 v18, v[64:67], s[10:11] offset:128
	v_pk_mul_f32 v[232:233], v[232:233], v[24:25] op_sel_hi:[1,0]
	v_pk_mul_f32 v[234:235], v[234:235], v[24:25] op_sel_hi:[1,0]
	v_pk_mul_f32 v[248:249], v[248:249], v[24:25] op_sel_hi:[1,0]
	v_pk_mul_f32 v[250:251], v[250:251], v[24:25] op_sel_hi:[1,0]
	v_pk_mul_f32 v[48:49], v[232:233], s[26:27]
	v_pk_mul_f32 v[50:51], v[234:235], s[26:27]
	v_pk_mul_f32 v[52:53], v[248:249], s[26:27]
	v_pk_mul_f32 v[54:55], v[250:251], s[26:27]
	v_pk_fma_f32 v[48:49], v[232:233], v[48:49], s[28:29] neg_lo:[1,0,0] neg_hi:[1,0,0]
	v_pk_fma_f32 v[50:51], v[234:235], v[50:51], s[28:29] neg_lo:[1,0,0] neg_hi:[1,0,0]
	v_pk_fma_f32 v[52:53], v[248:249], v[52:53], s[28:29] neg_lo:[1,0,0] neg_hi:[1,0,0]
	v_pk_fma_f32 v[54:55], v[250:251], v[54:55], s[28:29] neg_lo:[1,0,0] neg_hi:[1,0,0]
	v_pk_mul_f32 v[48:49], v[232:233], v[48:49]
	v_pk_mul_f32 v[50:51], v[234:235], v[50:51]
	v_pk_mul_f32 v[52:53], v[248:249], v[52:53]
	v_pk_mul_f32 v[54:55], v[250:251], v[54:55]
	v_exp_f32_e32 v48, v48
	v_exp_f32_e32 v49, v49
	v_exp_f32_e32 v50, v50
	v_exp_f32_e32 v51, v51
	v_exp_f32_e32 v52, v52
	v_exp_f32_e32 v53, v53
	v_exp_f32_e32 v54, v54
	v_exp_f32_e32 v55, v55
	v_pk_add_f32 v[48:49], v[48:49], s[30:31]
	v_pk_add_f32 v[50:51], v[50:51], s[30:31]
	v_pk_add_f32 v[52:53], v[52:53], s[30:31]
	v_pk_add_f32 v[54:55], v[54:55], s[30:31]
	v_rcp_f32_e32 v48, v48
	v_rcp_f32_e32 v49, v49
	v_rcp_f32_e32 v50, v50
	v_rcp_f32_e32 v51, v51
	v_rcp_f32_e32 v52, v52
	v_rcp_f32_e32 v53, v53
	v_rcp_f32_e32 v54, v54
	v_rcp_f32_e32 v55, v55
	s_nop 0
	v_pk_mul_f32 v[232:233], v[232:233], v[48:49]
	v_pk_mul_f32 v[234:235], v[234:235], v[50:51]
	v_pk_mul_f32 v[248:249], v[248:249], v[52:53]
	v_pk_mul_f32 v[250:251], v[250:251], v[54:55]
	v_cvt_pk_bf16_f32 v68, v232, v233
	v_cvt_pk_bf16_f32 v69, v234, v235
	v_cvt_pk_bf16_f32 v70, v248, v249
	v_cvt_pk_bf16_f32 v71, v250, v251
	s_nop 1
	v_permlane16_swap_b32 v68, v70
	v_permlane16_swap_b32 v69, v71
	global_store_dwordx4 v18, v[68:71], s[10:11] offset:192
	v_pk_mul_f32 v[140:141], v[140:141], v[26:27] op_sel_hi:[1,0]
	v_pk_mul_f32 v[142:143], v[142:143], v[26:27] op_sel_hi:[1,0]
	v_pk_mul_f32 v[156:157], v[156:157], v[26:27] op_sel_hi:[1,0]
	v_pk_mul_f32 v[158:159], v[158:159], v[26:27] op_sel_hi:[1,0]
	v_pk_mul_f32 v[32:33], v[140:141], s[26:27]
	v_pk_mul_f32 v[34:35], v[142:143], s[26:27]
	v_pk_mul_f32 v[36:37], v[156:157], s[26:27]
	v_pk_mul_f32 v[38:39], v[158:159], s[26:27]
	v_pk_fma_f32 v[32:33], v[140:141], v[32:33], s[28:29] neg_lo:[1,0,0] neg_hi:[1,0,0]
	v_pk_fma_f32 v[34:35], v[142:143], v[34:35], s[28:29] neg_lo:[1,0,0] neg_hi:[1,0,0]
	v_pk_fma_f32 v[36:37], v[156:157], v[36:37], s[28:29] neg_lo:[1,0,0] neg_hi:[1,0,0]
	v_pk_fma_f32 v[38:39], v[158:159], v[38:39], s[28:29] neg_lo:[1,0,0] neg_hi:[1,0,0]
	v_pk_mul_f32 v[32:33], v[140:141], v[32:33]
	v_pk_mul_f32 v[34:35], v[142:143], v[34:35]
	v_pk_mul_f32 v[36:37], v[156:157], v[36:37]
	v_pk_mul_f32 v[38:39], v[158:159], v[38:39]
	v_exp_f32_e32 v32, v32
	v_exp_f32_e32 v33, v33
	v_exp_f32_e32 v34, v34
	v_exp_f32_e32 v35, v35
	v_exp_f32_e32 v36, v36
	v_exp_f32_e32 v37, v37
	v_exp_f32_e32 v38, v38
	v_exp_f32_e32 v39, v39
	v_pk_add_f32 v[32:33], v[32:33], s[30:31]
	v_pk_add_f32 v[34:35], v[34:35], s[30:31]
	v_pk_add_f32 v[36:37], v[36:37], s[30:31]
	v_pk_add_f32 v[38:39], v[38:39], s[30:31]
	v_rcp_f32_e32 v32, v32
	v_rcp_f32_e32 v33, v33
	v_rcp_f32_e32 v34, v34
	v_rcp_f32_e32 v35, v35
	v_rcp_f32_e32 v36, v36
	v_rcp_f32_e32 v37, v37
	v_rcp_f32_e32 v38, v38
	v_rcp_f32_e32 v39, v39
	s_nop 0
	v_pk_mul_f32 v[140:141], v[140:141], v[32:33]
	v_pk_mul_f32 v[142:143], v[142:143], v[34:35]
	v_pk_mul_f32 v[156:157], v[156:157], v[36:37]
	v_pk_mul_f32 v[158:159], v[158:159], v[38:39]
	v_cvt_pk_bf16_f32 v64, v140, v141
	v_cvt_pk_bf16_f32 v65, v142, v143
	v_cvt_pk_bf16_f32 v66, v156, v157
	v_cvt_pk_bf16_f32 v67, v158, v159
	s_nop 1
	v_permlane16_swap_b32 v64, v66
	v_permlane16_swap_b32 v65, v67
	global_store_dwordx4 v19, v[64:67], s[10:11]
	v_pk_mul_f32 v[172:173], v[172:173], v[26:27] op_sel_hi:[1,0]
	v_pk_mul_f32 v[174:175], v[174:175], v[26:27] op_sel_hi:[1,0]
	v_pk_mul_f32 v[188:189], v[188:189], v[26:27] op_sel_hi:[1,0]
	v_pk_mul_f32 v[190:191], v[190:191], v[26:27] op_sel_hi:[1,0]
	v_pk_mul_f32 v[48:49], v[172:173], s[26:27]
	v_pk_mul_f32 v[50:51], v[174:175], s[26:27]
	v_pk_mul_f32 v[52:53], v[188:189], s[26:27]
	v_pk_mul_f32 v[54:55], v[190:191], s[26:27]
	v_pk_fma_f32 v[48:49], v[172:173], v[48:49], s[28:29] neg_lo:[1,0,0] neg_hi:[1,0,0]
	v_pk_fma_f32 v[50:51], v[174:175], v[50:51], s[28:29] neg_lo:[1,0,0] neg_hi:[1,0,0]
	v_pk_fma_f32 v[52:53], v[188:189], v[52:53], s[28:29] neg_lo:[1,0,0] neg_hi:[1,0,0]
	v_pk_fma_f32 v[54:55], v[190:191], v[54:55], s[28:29] neg_lo:[1,0,0] neg_hi:[1,0,0]
	v_pk_mul_f32 v[48:49], v[172:173], v[48:49]
	v_pk_mul_f32 v[50:51], v[174:175], v[50:51]
	v_pk_mul_f32 v[52:53], v[188:189], v[52:53]
	v_pk_mul_f32 v[54:55], v[190:191], v[54:55]
	v_exp_f32_e32 v48, v48
	v_exp_f32_e32 v49, v49
	v_exp_f32_e32 v50, v50
	v_exp_f32_e32 v51, v51
	v_exp_f32_e32 v52, v52
	v_exp_f32_e32 v53, v53
	v_exp_f32_e32 v54, v54
	v_exp_f32_e32 v55, v55
	v_pk_add_f32 v[48:49], v[48:49], s[30:31]
	v_pk_add_f32 v[50:51], v[50:51], s[30:31]
	v_pk_add_f32 v[52:53], v[52:53], s[30:31]
	v_pk_add_f32 v[54:55], v[54:55], s[30:31]
	v_rcp_f32_e32 v48, v48
	v_rcp_f32_e32 v49, v49
	v_rcp_f32_e32 v50, v50
	v_rcp_f32_e32 v51, v51
	v_rcp_f32_e32 v52, v52
	v_rcp_f32_e32 v53, v53
	v_rcp_f32_e32 v54, v54
	v_rcp_f32_e32 v55, v55
	s_nop 0
	v_pk_mul_f32 v[172:173], v[172:173], v[48:49]
	v_pk_mul_f32 v[174:175], v[174:175], v[50:51]
	v_pk_mul_f32 v[188:189], v[188:189], v[52:53]
	v_pk_mul_f32 v[190:191], v[190:191], v[54:55]
	v_cvt_pk_bf16_f32 v68, v172, v173
	v_cvt_pk_bf16_f32 v69, v174, v175
	v_cvt_pk_bf16_f32 v70, v188, v189
	v_cvt_pk_bf16_f32 v71, v190, v191
	s_nop 1
	v_permlane16_swap_b32 v68, v70
	v_permlane16_swap_b32 v69, v71
	global_store_dwordx4 v19, v[68:71], s[10:11] offset:64
	v_pk_mul_f32 v[204:205], v[204:205], v[26:27] op_sel_hi:[1,0]
	v_pk_mul_f32 v[206:207], v[206:207], v[26:27] op_sel_hi:[1,0]
	v_pk_mul_f32 v[220:221], v[220:221], v[26:27] op_sel_hi:[1,0]
	v_pk_mul_f32 v[222:223], v[222:223], v[26:27] op_sel_hi:[1,0]
	v_pk_mul_f32 v[32:33], v[204:205], s[26:27]
	v_pk_mul_f32 v[34:35], v[206:207], s[26:27]
	v_pk_mul_f32 v[36:37], v[220:221], s[26:27]
	v_pk_mul_f32 v[38:39], v[222:223], s[26:27]
	v_pk_fma_f32 v[32:33], v[204:205], v[32:33], s[28:29] neg_lo:[1,0,0] neg_hi:[1,0,0]
	v_pk_fma_f32 v[34:35], v[206:207], v[34:35], s[28:29] neg_lo:[1,0,0] neg_hi:[1,0,0]
	v_pk_fma_f32 v[36:37], v[220:221], v[36:37], s[28:29] neg_lo:[1,0,0] neg_hi:[1,0,0]
	v_pk_fma_f32 v[38:39], v[222:223], v[38:39], s[28:29] neg_lo:[1,0,0] neg_hi:[1,0,0]
	v_pk_mul_f32 v[32:33], v[204:205], v[32:33]
	v_pk_mul_f32 v[34:35], v[206:207], v[34:35]
	v_pk_mul_f32 v[36:37], v[220:221], v[36:37]
	v_pk_mul_f32 v[38:39], v[222:223], v[38:39]
	v_exp_f32_e32 v32, v32
	v_exp_f32_e32 v33, v33
	v_exp_f32_e32 v34, v34
	v_exp_f32_e32 v35, v35
	v_exp_f32_e32 v36, v36
	v_exp_f32_e32 v37, v37
	v_exp_f32_e32 v38, v38
	v_exp_f32_e32 v39, v39
	v_pk_add_f32 v[32:33], v[32:33], s[30:31]
	v_pk_add_f32 v[34:35], v[34:35], s[30:31]
	v_pk_add_f32 v[36:37], v[36:37], s[30:31]
	v_pk_add_f32 v[38:39], v[38:39], s[30:31]
	v_rcp_f32_e32 v32, v32
	v_rcp_f32_e32 v33, v33
	v_rcp_f32_e32 v34, v34
	v_rcp_f32_e32 v35, v35
	v_rcp_f32_e32 v36, v36
	v_rcp_f32_e32 v37, v37
	v_rcp_f32_e32 v38, v38
	v_rcp_f32_e32 v39, v39
	s_nop 0
	v_pk_mul_f32 v[204:205], v[204:205], v[32:33]
	v_pk_mul_f32 v[206:207], v[206:207], v[34:35]
	v_pk_mul_f32 v[220:221], v[220:221], v[36:37]
	v_pk_mul_f32 v[222:223], v[222:223], v[38:39]
	v_cvt_pk_bf16_f32 v64, v204, v205
	v_cvt_pk_bf16_f32 v65, v206, v207
	v_cvt_pk_bf16_f32 v66, v220, v221
	v_cvt_pk_bf16_f32 v67, v222, v223
	s_nop 1
	v_permlane16_swap_b32 v64, v66
	v_permlane16_swap_b32 v65, v67
	global_store_dwordx4 v19, v[64:67], s[10:11] offset:128
	v_pk_mul_f32 v[236:237], v[236:237], v[26:27] op_sel_hi:[1,0]
	v_pk_mul_f32 v[238:239], v[238:239], v[26:27] op_sel_hi:[1,0]
	v_pk_mul_f32 v[252:253], v[252:253], v[26:27] op_sel_hi:[1,0]
	v_pk_mul_f32 v[254:255], v[254:255], v[26:27] op_sel_hi:[1,0]
	v_pk_mul_f32 v[48:49], v[236:237], s[26:27]
	v_pk_mul_f32 v[50:51], v[238:239], s[26:27]
	v_pk_mul_f32 v[52:53], v[252:253], s[26:27]
	v_pk_mul_f32 v[54:55], v[254:255], s[26:27]
	v_pk_fma_f32 v[48:49], v[236:237], v[48:49], s[28:29] neg_lo:[1,0,0] neg_hi:[1,0,0]
	v_pk_fma_f32 v[50:51], v[238:239], v[50:51], s[28:29] neg_lo:[1,0,0] neg_hi:[1,0,0]
	v_pk_fma_f32 v[52:53], v[252:253], v[52:53], s[28:29] neg_lo:[1,0,0] neg_hi:[1,0,0]
	v_pk_fma_f32 v[54:55], v[254:255], v[54:55], s[28:29] neg_lo:[1,0,0] neg_hi:[1,0,0]
	v_pk_mul_f32 v[48:49], v[236:237], v[48:49]
	v_pk_mul_f32 v[50:51], v[238:239], v[50:51]
	v_pk_mul_f32 v[52:53], v[252:253], v[52:53]
	v_pk_mul_f32 v[54:55], v[254:255], v[54:55]
	v_exp_f32_e32 v48, v48
	v_exp_f32_e32 v49, v49
	v_exp_f32_e32 v50, v50
	v_exp_f32_e32 v51, v51
	v_exp_f32_e32 v52, v52
	v_exp_f32_e32 v53, v53
	v_exp_f32_e32 v54, v54
	v_exp_f32_e32 v55, v55
	v_pk_add_f32 v[48:49], v[48:49], s[30:31]
	v_pk_add_f32 v[50:51], v[50:51], s[30:31]
	v_pk_add_f32 v[52:53], v[52:53], s[30:31]
	v_pk_add_f32 v[54:55], v[54:55], s[30:31]
	v_rcp_f32_e32 v48, v48
	v_rcp_f32_e32 v49, v49
	v_rcp_f32_e32 v50, v50
	v_rcp_f32_e32 v51, v51
	v_rcp_f32_e32 v52, v52
	v_rcp_f32_e32 v53, v53
	v_rcp_f32_e32 v54, v54
	v_rcp_f32_e32 v55, v55
	s_nop 0
	v_pk_mul_f32 v[236:237], v[236:237], v[48:49]
	v_pk_mul_f32 v[238:239], v[238:239], v[50:51]
	v_pk_mul_f32 v[252:253], v[252:253], v[52:53]
	v_pk_mul_f32 v[254:255], v[254:255], v[54:55]
	v_cvt_pk_bf16_f32 v68, v236, v237
	v_cvt_pk_bf16_f32 v69, v238, v239
	v_cvt_pk_bf16_f32 v70, v252, v253
	v_cvt_pk_bf16_f32 v71, v254, v255
	s_nop 1
	v_permlane16_swap_b32 v68, v70
	v_permlane16_swap_b32 v69, v71
	global_store_dwordx4 v19, v[68:71], s[10:11] offset:192
